# attention steps: address-copy v_mov before K/V, CV loads and CV store removed (use the loop-invariant VGPR directly)
# speedup vs baseline: 1.0164x; 1.0060x over previous
; DI void finishSM(f32x16& p0, f32x16& p1, float alpha, float& l_reg, bf16x8& pa0, bf16x8& pa1, bf16x8& pa2, bf16x8& pa3) {
; #pragma unroll
;     for (int r = 0; r < 16; ++r) p1[r] = __builtin_amdgcn_exp2f(p1[r]);
;     float ps = 0;
; #pragma unroll
;     for (int r = 0; r < 16; ++r) ps += p0[r];
; #pragma unroll
;     for (int r = 0; r < 16; ++r) ps += p1[r];
;     { auto rr = __builtin_amdgcn_permlane32_swap(__float_as_uint(ps), __float_as_uint(ps), false, false); ps = __uint_as_float(rr[0]) + __uint_as_float(rr[1]); }
;     l_reg = l_reg * alpha + ps;
;     ...
;     AT_PK4(p0, 0, pa0); AT_PK4(p0, 8, pa1); AT_PK4(p1, 0, pa2); AT_PK4(p1, 8, pa3);
;     ...
; }
; DI void qkt(f32x16& p0, f32x16& p1, const char* Ks, const bf16x8* qr, const f32x16& negm, int r32, int hi) {
; #pragma unroll
;     for (int d0 = 0; d0 < 4; ++d0) { const int cb = (d0 * 16 + hi * 8) * 2;
;         const bf16x8 b0 = *reinterpret_cast<const bf16x8*>(Ks + AT_KSWZ(r32, cb));
;         const bf16x8 b1 = *reinterpret_cast<const bf16x8*>(Ks + AT_KSWZ(32 + r32, cb));
;         p0 = __builtin_amdgcn_mfma_f32_32x32x16_bf16(b0, qr[d0], d0 == 0 ? negm : p0, 0, 0, 0);
;         p1 = __builtin_amdgcn_mfma_f32_32x32x16_bf16(b1, qr[d0], d0 == 0 ? negm : p1, 0, 0, 0); }
; DI void attn_pass(const Frame& F, CvRide& cv, const bf16_t* __restrict__ Qb, const bf16_t* __restrict__ Kh, const bf16_t* __restrict__ Vh, char* lds, f32x16 (&o)[4], float& l_out, const int wave_s) {
;     ...
;     const unsigned cv_ldo = (unsigned)(((tid >> 4) * 2 * 2048 + (tid & 15) * 4) * 4), cv_sto = (unsigned)((tid >> 3) * 2048 + 8 * (tid & 7));
;     const int cv_lw = OFF_CV + (4 * (tid & 15)) * 68 + 2 * (tid >> 4), cv_lr = OFF_CV + (tid >> 3) * 68 + 8 * (tid & 7);
;     f32x4 cvA = f32x4{}, cvB = f32x4{}; unsigned cvr0 = 0, cvr1 = 0;
.LBB4_701:
	s_lshl_b32 s26, s58, 8
	s_and_b32 s26, s26, 0x1f00
	s_add_u32 s74, s12, s26
	s_addc_u32 s75, s13, 0
	s_add_u32 s76, s74, 0x2000
	s_addc_u32 s77, s75, 0
	global_load_dwordx4 v[160:163], v209, s[74:75] nt
	global_load_dwordx4 v[164:167], v209, s[76:77] nt
.LBB4_702:
	s_lshl_b32 s26, s66, 13
	s_add_i32 s26, s26, 0
	v_add_u32_e32 v72, s26, v205
	v_add_u32_e32 v112, s26, v206
	v_add_u32_e32 v180, s26, v207
	s_waitcnt lgkmcnt(1)
	v_mfma_f32_32x32x16_bf16 v[128:143], v[64:67], v[156:159], v[80:95]
	ds_read_b128 v[64:67], v72 offset:49152
	ds_read_b128 v[72:75], v72 offset:53248
	ds_read_b128 v[76:79], v112 offset:49152
	ds_read_b128 v[220:223], v112 offset:53248
	v_exp_f32_e32 v186, v97
	v_exp_f32_e32 v213, v98
	v_exp_f32_e32 v214, v99
	v_exp_f32_e32 v219, v100
	v_exp_f32_e32 v228, v101
	s_waitcnt lgkmcnt(4)
	v_mfma_f32_32x32x16_bf16 v[112:127], v[68:71], v[156:159], v[80:95]
	ds_read_b128 v[68:71], v180 offset:49152
	ds_read_b128 v[224:227], v180 offset:53248
	v_exp_f32_e32 v180, v96
	v_cvt_pk_bf16_f32 v96, v216, v218
	v_cvt_pk_bf16_f32 v97, v179, v217
	v_cvt_pk_bf16_f32 v98, v177, v215
	v_cvt_pk_bf16_f32 v99, v176, v178
	s_waitcnt lgkmcnt(4)
	v_mfma_f32_32x32x16_bf16 v[112:127], v[72:75], v[152:155], v[112:127]
	v_add_f32_e32 v75, 0, v216
	v_add_f32_e32 v75, v218, v75
	v_add_f32_e32 v75, v179, v75
	v_add_f32_e32 v75, v217, v75
	v_add_f32_e32 v75, v177, v75
	v_add_f32_e32 v75, v215, v75
	v_add_f32_e32 v75, v176, v75
	v_mfma_f32_32x32x16_bf16 v[128:143], v[64:67], v[152:155], v[128:143]
	v_add_f32_e32 v75, v178, v75
	v_add_f32_e32 v75, v173, v75
	v_add_f32_e32 v75, v175, v75
	v_add_f32_e32 v75, v171, v75
	v_add_f32_e32 v75, v174, v75
	v_add_f32_e32 v75, v169, v75
	v_add_f32_e32 v75, v172, v75
	s_waitcnt lgkmcnt(3)
	v_mfma_f32_32x32x16_bf16 v[128:143], v[76:79], v[148:151], v[128:143]
	v_add_f32_e32 v75, v168, v75
	v_add_f32_e32 v75, v170, v75
	v_add_f32_e32 v75, v180, v75
	v_add_f32_e32 v75, v186, v75
	v_exp_f32_e32 v64, v102
	v_exp_f32_e32 v65, v103
	v_exp_f32_e32 v66, v104
	s_waitcnt lgkmcnt(2)
	v_mfma_f32_32x32x16_bf16 v[112:127], v[220:223], v[148:151], v[112:127]
	v_exp_f32_e32 v67, v105
	v_exp_f32_e32 v105, v106
	v_exp_f32_e32 v106, v107
	v_exp_f32_e32 v107, v108
	v_exp_f32_e32 v72, v109
	v_exp_f32_e32 v73, v110
	v_exp_f32_e32 v74, v111
	s_waitcnt lgkmcnt(1)
	v_mfma_f32_32x32x16_bf16 v[128:143], v[68:71], v[144:147], v[128:143]
	v_add_f32_e32 v68, v213, v75
	v_add_f32_e32 v68, v214, v68
	v_add_f32_e32 v68, v219, v68
	v_add_f32_e32 v68, v228, v68
	v_add_f32_e32 v68, v64, v68
	v_add_f32_e32 v68, v65, v68
	v_add_f32_e32 v68, v66, v68
	v_add_f32_e32 v68, v67, v68
	s_waitcnt lgkmcnt(0)
	v_mfma_f32_32x32x16_bf16 v[112:127], v[224:227], v[144:147], v[112:127]
	v_add_f32_e32 v68, v105, v68
	v_add_f32_e32 v68, v106, v68
	v_add_f32_e32 v68, v107, v68
	v_add_f32_e32 v68, v72, v68
	v_add_f32_e32 v68, v73, v68
	v_add_f32_e32 v183, v74, v68
	v_mov_b32_e32 v212, v183
	v_cvt_pk_bf16_f32 v108, v173, v175
	v_cvt_pk_bf16_f32 v109, v171, v174
	v_cvt_pk_bf16_f32 v110, v169, v172
	v_cvt_pk_bf16_f32 v111, v168, v170
	v_cvt_pk_bf16_f32 v100, v180, v186
	v_cvt_pk_bf16_f32 v101, v213, v214
	v_cvt_pk_bf16_f32 v102, v219, v228
	v_cvt_pk_bf16_f32 v103, v64, v65
	v_cvt_pk_bf16_f32 v104, v66, v67
	v_cvt_pk_bf16_f32 v105, v105, v106
	v_cvt_pk_bf16_f32 v106, v107, v72
	v_cvt_pk_bf16_f32 v107, v73, v74
	s_nop 1
	v_permlane32_swap_b32_e32 v183, v212
	v_permlane32_swap_b32_e32 v96, v98
	v_permlane32_swap_b32_e32 v97, v99
	v_permlane32_swap_b32_e32 v108, v110
	v_permlane32_swap_b32_e32 v109, v111
	v_permlane32_swap_b32_e32 v100, v102
	v_permlane32_swap_b32_e32 v101, v103
	v_permlane32_swap_b32_e32 v104, v106
	v_permlane32_swap_b32_e32 v105, v107
	s_add_u32 s74, s46, s28
	s_addc_u32 s75, s47, s29
	s_add_u32 s78, s74, 0x23808000
	s_addc_u32 s79, s75, 0
	s_add_u32 s80, s74, 0x2380a000
	s_addc_u32 s81, s75, 0
	s_add_u32 s76, s46, s30
	s_addc_u32 s77, s47, s31
	s_add_u32 s82, s76, 0x21804000
	s_addc_u32 s83, s77, 0
	global_load_dwordx4 v[176:179], v197, s[78:79]
	global_load_dwordx4 v[172:175], v197, s[80:81]
	global_load_dwordx4 v[168:171], v198, s[82:83]
	s_andn2_b64 vcc, exec, s[2:3]
	s_cbranch_vccnz .LBB4_704
	s_mov_b64 s[2:3], s[8:9]
	global_store_dwordx2 v189, v[184:185], s[2:3] nt

; DI void finishSM(f32x16& p0, f32x16& p1, float alpha, float& l_reg, bf16x8& pa0, bf16x8& pa1, bf16x8& pa2, bf16x8& pa3) {
; #pragma unroll
;     for (int r = 0; r < 16; ++r) p1[r] = __builtin_amdgcn_exp2f(p1[r]);
;     float ps = 0;
; #pragma unroll
;     for (int r = 0; r < 16; ++r) ps += p0[r];
; #pragma unroll
;     for (int r = 0; r < 16; ++r) ps += p1[r];
;     { auto rr = __builtin_amdgcn_permlane32_swap(__float_as_uint(ps), __float_as_uint(ps), false, false); ps = __uint_as_float(rr[0]) + __uint_as_float(rr[1]); }
;     l_reg = l_reg * alpha + ps;
;     ...
;     AT_PK4(p0, 0, pa0); AT_PK4(p0, 8, pa1); AT_PK4(p1, 0, pa2); AT_PK4(p1, 8, pa3);
;     ...
; }
; DI void qkt(f32x16& p0, f32x16& p1, const char* Ks, const bf16x8* qr, const f32x16& negm, int r32, int hi) {
; #pragma unroll
;     for (int d0 = 0; d0 < 4; ++d0) { const int cb = (d0 * 16 + hi * 8) * 2;
;         const bf16x8 b0 = *reinterpret_cast<const bf16x8*>(Ks + AT_KSWZ(r32, cb));
;         const bf16x8 b1 = *reinterpret_cast<const bf16x8*>(Ks + AT_KSWZ(32 + r32, cb));
;         p0 = __builtin_amdgcn_mfma_f32_32x32x16_bf16(b0, qr[d0], d0 == 0 ? negm : p0, 0, 0, 0);
;         p1 = __builtin_amdgcn_mfma_f32_32x32x16_bf16(b1, qr[d0], d0 == 0 ? negm : p1, 0, 0, 0); }
; DI void attn_pass(const Frame& F, CvRide& cv, const bf16_t* __restrict__ Qb, const bf16_t* __restrict__ Kh, const bf16_t* __restrict__ Vh, char* lds, f32x16 (&o)[4], float& l_out, const int wave_s) {
;     ...
;     const unsigned cv_ldo = (unsigned)(((tid >> 4) * 2 * 2048 + (tid & 15) * 4) * 4), cv_sto = (unsigned)((tid >> 3) * 2048 + 8 * (tid & 7));
;     const int cv_lw = OFF_CV + (4 * (tid & 15)) * 68 + 2 * (tid >> 4), cv_lr = OFF_CV + (tid >> 3) * 68 + 8 * (tid & 7);
;     f32x4 cvA = f32x4{}, cvB = f32x4{}; unsigned cvr0 = 0, cvr1 = 0;
.LBB4_722:
	s_lshl_b32 s26, s58, 8
	s_and_b32 s26, s26, 0x1f00
	s_add_u32 s80, s12, s26
	s_addc_u32 s81, s13, 0
	s_add_u32 s82, s80, 0x2000
	s_addc_u32 s83, s81, 0
	global_load_dwordx4 v[160:163], v209, s[80:81] nt
	global_load_dwordx4 v[164:167], v209, s[82:83] nt
.LBB4_723:
	v_exp_f32_e32 v186, v128
	v_exp_f32_e32 v230, v129
	v_exp_f32_e32 v231, v130
	v_exp_f32_e32 v232, v131
	v_exp_f32_e32 v233, v132
	v_exp_f32_e32 v234, v133
	v_exp_f32_e32 v235, v134
	v_exp_f32_e32 v236, v135
	v_exp_f32_e32 v237, v136
	v_exp_f32_e32 v238, v137
	v_exp_f32_e32 v239, v138
	v_exp_f32_e32 v240, v139
	v_exp_f32_e32 v241, v140
	v_exp_f32_e32 v242, v141
	v_exp_f32_e32 v243, v142
	v_exp_f32_e32 v244, v143
	v_add_u32_e32 v101, s78, v205
	v_add_u32_e32 v102, s78, v206
	v_add_u32_e32 v103, s78, v207
	ds_read_b128 v[172:175], v101 offset:49152
	ds_read_b128 v[176:179], v101 offset:53248
	ds_read_b128 v[214:217], v102 offset:49152
	ds_read_b128 v[218:221], v102 offset:53248
	ds_read_b128 v[222:225], v103 offset:49152
	ds_read_b128 v[226:229], v103 offset:53248
	v_exp_f32_e32 v112, v112
	v_exp_f32_e32 v113, v113
	v_exp_f32_e32 v114, v114
	s_waitcnt lgkmcnt(7)
	v_mfma_f32_32x32x16_bf16 v[128:143], v[96:99], v[156:159], v[80:95]
	v_exp_f32_e32 v115, v115
	v_exp_f32_e32 v116, v116
	v_exp_f32_e32 v117, v117
	v_exp_f32_e32 v118, v118
	v_exp_f32_e32 v119, v119
	s_waitcnt lgkmcnt(6)
	v_mfma_f32_32x32x16_bf16 v[96:111], v[168:171], v[156:159], v[80:95]
	v_exp_f32_e32 v168, v120
	v_add_f32_e32 v120, 0, v186
	v_add_f32_e32 v120, v230, v120
	v_add_f32_e32 v120, v231, v120
	v_add_f32_e32 v120, v232, v120
	v_add_f32_e32 v120, v233, v120
	v_add_f32_e32 v120, v234, v120
	v_add_f32_e32 v120, v235, v120
	v_add_f32_e32 v120, v236, v120
	v_add_f32_e32 v120, v237, v120
	v_add_f32_e32 v120, v238, v120
	s_waitcnt lgkmcnt(5)
	v_mfma_f32_32x32x16_bf16 v[128:143], v[172:175], v[152:155], v[128:143]
	v_add_f32_e32 v120, v239, v120
	v_add_f32_e32 v120, v240, v120
	v_add_f32_e32 v120, v241, v120
	v_add_f32_e32 v120, v242, v120
	v_add_f32_e32 v120, v243, v120
	v_add_f32_e32 v120, v244, v120
	v_add_f32_e32 v120, v112, v120
	s_waitcnt lgkmcnt(4)
	v_mfma_f32_32x32x16_bf16 v[96:111], v[176:179], v[152:155], v[96:111]
	v_add_f32_e32 v120, v113, v120
	v_add_f32_e32 v120, v114, v120
	v_add_f32_e32 v120, v115, v120
	v_add_f32_e32 v120, v116, v120
	v_exp_f32_e32 v169, v121
	v_add_f32_e32 v120, v117, v120
	v_exp_f32_e32 v170, v122
	s_waitcnt lgkmcnt(3)
	v_mfma_f32_32x32x16_bf16 v[128:143], v[214:217], v[148:151], v[128:143]
	v_add_f32_e32 v120, v118, v120
	v_exp_f32_e32 v171, v123
	v_add_f32_e32 v120, v119, v120
	v_exp_f32_e32 v172, v124
	v_add_f32_e32 v120, v168, v120
	v_exp_f32_e32 v173, v125
	v_add_f32_e32 v120, v169, v120
	s_waitcnt lgkmcnt(2)
	v_mfma_f32_32x32x16_bf16 v[96:111], v[218:221], v[148:151], v[96:111]
	v_exp_f32_e32 v174, v126
	v_add_f32_e32 v120, v170, v120
	v_exp_f32_e32 v175, v127
	v_add_f32_e32 v120, v171, v120
	v_add_f32_e32 v120, v172, v120
	v_add_f32_e32 v120, v173, v120
	v_add_f32_e32 v120, v174, v120
	s_waitcnt lgkmcnt(1)
	v_mfma_f32_32x32x16_bf16 v[128:143], v[222:225], v[144:147], v[128:143]
	v_add_f32_e32 v213, v175, v120
	v_mov_b32_e32 v214, v213
	v_cvt_pk_bf16_f32 v120, v186, v230
	v_cvt_pk_bf16_f32 v121, v231, v232
	v_cvt_pk_bf16_f32 v122, v233, v234
	v_cvt_pk_bf16_f32 v123, v235, v236
	v_cvt_pk_bf16_f32 v124, v237, v238
	s_waitcnt lgkmcnt(0)
	v_mfma_f32_32x32x16_bf16 v[96:111], v[226:229], v[144:147], v[96:111]
	v_cvt_pk_bf16_f32 v125, v239, v240
	v_cvt_pk_bf16_f32 v126, v241, v242
	v_cvt_pk_bf16_f32 v127, v243, v244
	v_cvt_pk_bf16_f32 v112, v112, v113
	v_cvt_pk_bf16_f32 v113, v114, v115
	v_cvt_pk_bf16_f32 v114, v116, v117
	v_cvt_pk_bf16_f32 v115, v118, v119
	v_cvt_pk_bf16_f32 v116, v168, v169
	v_cvt_pk_bf16_f32 v117, v170, v171
	v_cvt_pk_bf16_f32 v118, v172, v173
	v_cvt_pk_bf16_f32 v119, v174, v175
	v_permlane32_swap_b32_e32 v213, v214
	v_permlane32_swap_b32_e32 v120, v122
	v_permlane32_swap_b32_e32 v121, v123
	v_permlane32_swap_b32_e32 v124, v126
	v_permlane32_swap_b32_e32 v125, v127
	v_permlane32_swap_b32_e32 v112, v114
	v_permlane32_swap_b32_e32 v113, v115
	v_permlane32_swap_b32_e32 v116, v118
	v_permlane32_swap_b32_e32 v117, v119
	s_add_u32 s78, s74, 0x2380c000
	s_addc_u32 s79, s75, 0
	s_add_u32 s74, s74, 0x2380e000
	s_addc_u32 s75, s75, 0
	s_add_u32 s76, s76, 0x21806000
	s_addc_u32 s77, s77, 0
	global_load_dwordx4 v[176:179], v197, s[78:79]
	global_load_dwordx4 v[172:175], v197, s[74:75]
	s_nop 0
	global_load_dwordx4 v[168:171], v198, s[76:77]
	s_and_b64 vcc, exec, s[2:3]
	s_cbranch_vccnz .LBB4_725
	s_mov_b64 s[2:3], s[8:9]
	global_store_dwordx2 v189, v[184:185], s[2:3] nt

; DI void finishSM(f32x16& p0, f32x16& p1, float alpha, float& l_reg, bf16x8& pa0, bf16x8& pa1, bf16x8& pa2, bf16x8& pa3) {
; #pragma unroll
;     for (int r = 0; r < 16; ++r) p1[r] = __builtin_amdgcn_exp2f(p1[r]);
;     float ps = 0;
; #pragma unroll
;     for (int r = 0; r < 16; ++r) ps += p0[r];
; #pragma unroll
;     for (int r = 0; r < 16; ++r) ps += p1[r];
;     { auto rr = __builtin_amdgcn_permlane32_swap(__float_as_uint(ps), __float_as_uint(ps), false, false); ps = __uint_as_float(rr[0]) + __uint_as_float(rr[1]); }
;     l_reg = l_reg * alpha + ps;
;     ...
;     AT_PK4(p0, 0, pa0); AT_PK4(p0, 8, pa1); AT_PK4(p1, 0, pa2); AT_PK4(p1, 8, pa3);
;     ...
; }
; DI void qkt(f32x16& p0, f32x16& p1, const char* Ks, const bf16x8* qr, const f32x16& negm, int r32, int hi) {
; #pragma unroll
;     for (int d0 = 0; d0 < 4; ++d0) { const int cb = (d0 * 16 + hi * 8) * 2;
;         const bf16x8 b0 = *reinterpret_cast<const bf16x8*>(Ks + AT_KSWZ(r32, cb));
;         const bf16x8 b1 = *reinterpret_cast<const bf16x8*>(Ks + AT_KSWZ(32 + r32, cb));
;         p0 = __builtin_amdgcn_mfma_f32_32x32x16_bf16(b0, qr[d0], d0 == 0 ? negm : p0, 0, 0, 0);
;         p1 = __builtin_amdgcn_mfma_f32_32x32x16_bf16(b1, qr[d0], d0 == 0 ? negm : p1, 0, 0, 0); }
; DI void attn_pass(const Frame& F, CvRide& cv, const bf16_t* __restrict__ Qb, const bf16_t* __restrict__ Kh, const bf16_t* __restrict__ Vh, char* lds, f32x16 (&o)[4], float& l_out, const int wave_s) {
;     ...
;     const unsigned cv_ldo = (unsigned)(((tid >> 4) * 2 * 2048 + (tid & 15) * 4) * 4), cv_sto = (unsigned)((tid >> 3) * 2048 + 8 * (tid & 7));
;     const int cv_lw = OFF_CV + (4 * (tid & 15)) * 68 + 2 * (tid >> 4), cv_lr = OFF_CV + (tid >> 3) * 68 + 8 * (tid & 7);
;     f32x4 cvA = f32x4{}, cvB = f32x4{}; unsigned cvr0 = 0, cvr1 = 0;
.LBB4_774:
	s_lshl_b32 s20, s58, 8
	s_and_b32 s20, s20, 0x1f00
	s_add_u32 s24, s12, s20
	s_addc_u32 s25, s13, 0
	s_add_u32 s34, s24, 0x2000
	s_addc_u32 s35, s25, 0
	global_load_dwordx4 v[160:163], v213, s[24:25] nt
	global_load_dwordx4 v[164:167], v213, s[34:35] nt
.LBB4_775:
	s_lshl_b32 s20, s30, 13
	s_add_i32 s20, s20, 0
	v_add_u32_e32 v72, s20, v208
	v_add_u32_e32 v112, s20, v209
	v_add_u32_e32 v180, s20, v210
	s_waitcnt lgkmcnt(1)
	v_mfma_f32_32x32x16_bf16 v[128:143], v[64:67], v[156:159], v[80:95]
	ds_read_b128 v[64:67], v72 offset:49152
	ds_read_b128 v[72:75], v72 offset:53248
	ds_read_b128 v[76:79], v112 offset:49152
	ds_read_b128 v[224:227], v112 offset:53248
	v_exp_f32_e32 v182, v97
	v_exp_f32_e32 v217, v98
	v_exp_f32_e32 v218, v99
	v_exp_f32_e32 v223, v100
	v_exp_f32_e32 v232, v101
	s_waitcnt lgkmcnt(4)
	v_mfma_f32_32x32x16_bf16 v[112:127], v[68:71], v[156:159], v[80:95]
	ds_read_b128 v[68:71], v180 offset:49152
	ds_read_b128 v[228:231], v180 offset:53248
	v_exp_f32_e32 v180, v96
	v_cvt_pk_bf16_f32 v96, v220, v222
	v_cvt_pk_bf16_f32 v97, v179, v221
	v_cvt_pk_bf16_f32 v98, v177, v219
	v_cvt_pk_bf16_f32 v99, v176, v178
	s_waitcnt lgkmcnt(4)
	v_mfma_f32_32x32x16_bf16 v[112:127], v[72:75], v[152:155], v[112:127]
	v_add_f32_e32 v75, 0, v220
	v_add_f32_e32 v75, v222, v75
	v_add_f32_e32 v75, v179, v75
	v_add_f32_e32 v75, v221, v75
	v_add_f32_e32 v75, v177, v75
	v_add_f32_e32 v75, v219, v75
	v_add_f32_e32 v75, v176, v75
	v_mfma_f32_32x32x16_bf16 v[128:143], v[64:67], v[152:155], v[128:143]
	v_add_f32_e32 v75, v178, v75
	v_add_f32_e32 v75, v173, v75
	v_add_f32_e32 v75, v175, v75
	v_add_f32_e32 v75, v171, v75
	v_add_f32_e32 v75, v174, v75
	v_add_f32_e32 v75, v169, v75
	v_add_f32_e32 v75, v172, v75
	s_waitcnt lgkmcnt(3)
	v_mfma_f32_32x32x16_bf16 v[128:143], v[76:79], v[148:151], v[128:143]
	v_add_f32_e32 v75, v168, v75
	v_add_f32_e32 v75, v170, v75
	v_add_f32_e32 v75, v180, v75
	v_add_f32_e32 v75, v182, v75
	v_exp_f32_e32 v64, v102
	v_exp_f32_e32 v65, v103
	v_exp_f32_e32 v66, v104
	s_waitcnt lgkmcnt(2)
	v_mfma_f32_32x32x16_bf16 v[112:127], v[224:227], v[148:151], v[112:127]
	v_exp_f32_e32 v67, v105
	v_exp_f32_e32 v105, v106
	v_exp_f32_e32 v106, v107
	v_exp_f32_e32 v107, v108
	v_exp_f32_e32 v72, v109
	v_exp_f32_e32 v73, v110
	v_exp_f32_e32 v74, v111
	s_waitcnt lgkmcnt(1)
	v_mfma_f32_32x32x16_bf16 v[128:143], v[68:71], v[144:147], v[128:143]
	v_add_f32_e32 v68, v217, v75
	v_add_f32_e32 v68, v218, v68
	v_add_f32_e32 v68, v223, v68
	v_add_f32_e32 v68, v232, v68
	v_add_f32_e32 v68, v64, v68
	v_add_f32_e32 v68, v65, v68
	v_add_f32_e32 v68, v66, v68
	v_add_f32_e32 v68, v67, v68
	s_waitcnt lgkmcnt(0)
	v_mfma_f32_32x32x16_bf16 v[112:127], v[228:231], v[144:147], v[112:127]
	v_add_f32_e32 v68, v105, v68
	v_add_f32_e32 v68, v106, v68
	v_add_f32_e32 v68, v107, v68
	v_add_f32_e32 v68, v72, v68
	v_add_f32_e32 v68, v73, v68
	v_add_f32_e32 v215, v74, v68
	v_mov_b32_e32 v216, v215
	v_cvt_pk_bf16_f32 v108, v173, v175
	v_cvt_pk_bf16_f32 v109, v171, v174
	v_cvt_pk_bf16_f32 v110, v169, v172
	v_cvt_pk_bf16_f32 v111, v168, v170
	v_cvt_pk_bf16_f32 v100, v180, v182
	v_cvt_pk_bf16_f32 v101, v217, v218
	v_cvt_pk_bf16_f32 v102, v223, v232
	v_cvt_pk_bf16_f32 v103, v64, v65
	v_cvt_pk_bf16_f32 v104, v66, v67
	v_cvt_pk_bf16_f32 v105, v105, v106
	v_cvt_pk_bf16_f32 v106, v107, v72
	v_cvt_pk_bf16_f32 v107, v73, v74
	s_nop 1
	v_permlane32_swap_b32_e32 v215, v216
	v_permlane32_swap_b32_e32 v96, v98
	v_permlane32_swap_b32_e32 v97, v99
	v_permlane32_swap_b32_e32 v108, v110
	v_permlane32_swap_b32_e32 v109, v111
	v_permlane32_swap_b32_e32 v100, v102
	v_permlane32_swap_b32_e32 v101, v103
	v_permlane32_swap_b32_e32 v104, v106
	v_permlane32_swap_b32_e32 v105, v107
	s_add_u32 s34, s46, s16
	s_addc_u32 s35, s47, s17
	s_add_u32 s24, s34, 0x23808000
	s_addc_u32 s25, s35, 0
	s_add_u32 s66, s34, 0x2380a000
	s_addc_u32 s67, s35, 0
	s_add_u32 s37, s46, s18
	s_addc_u32 s64, s47, s19
	s_add_u32 s74, s37, 0x21884000
	s_addc_u32 s75, s64, 0
	global_load_dwordx4 v[176:179], v200, s[24:25]
	global_load_dwordx4 v[172:175], v200, s[66:67]
	global_load_dwordx4 v[168:171], v201, s[74:75]
	s_andn2_b64 vcc, exec, s[2:3]
	s_cbranch_vccnz .LBB4_777
	s_mov_b64 s[2:3], s[8:9]
	global_store_dwordx2 v193, v[184:185], s[2:3] nt

; DI void finishSM(f32x16& p0, f32x16& p1, float alpha, float& l_reg, bf16x8& pa0, bf16x8& pa1, bf16x8& pa2, bf16x8& pa3) {
; #pragma unroll
;     for (int r = 0; r < 16; ++r) p1[r] = __builtin_amdgcn_exp2f(p1[r]);
;     float ps = 0;
; #pragma unroll
;     for (int r = 0; r < 16; ++r) ps += p0[r];
; #pragma unroll
;     for (int r = 0; r < 16; ++r) ps += p1[r];
;     { auto rr = __builtin_amdgcn_permlane32_swap(__float_as_uint(ps), __float_as_uint(ps), false, false); ps = __uint_as_float(rr[0]) + __uint_as_float(rr[1]); }
;     l_reg = l_reg * alpha + ps;
;     ...
;     AT_PK4(p0, 0, pa0); AT_PK4(p0, 8, pa1); AT_PK4(p1, 0, pa2); AT_PK4(p1, 8, pa3);
;     ...
; }
; DI void qkt(f32x16& p0, f32x16& p1, const char* Ks, const bf16x8* qr, const f32x16& negm, int r32, int hi) {
; #pragma unroll
;     for (int d0 = 0; d0 < 4; ++d0) { const int cb = (d0 * 16 + hi * 8) * 2;
;         const bf16x8 b0 = *reinterpret_cast<const bf16x8*>(Ks + AT_KSWZ(r32, cb));
;         const bf16x8 b1 = *reinterpret_cast<const bf16x8*>(Ks + AT_KSWZ(32 + r32, cb));
;         p0 = __builtin_amdgcn_mfma_f32_32x32x16_bf16(b0, qr[d0], d0 == 0 ? negm : p0, 0, 0, 0);
;         p1 = __builtin_amdgcn_mfma_f32_32x32x16_bf16(b1, qr[d0], d0 == 0 ? negm : p1, 0, 0, 0); }
; DI void attn_pass(const Frame& F, CvRide& cv, const bf16_t* __restrict__ Qb, const bf16_t* __restrict__ Kh, const bf16_t* __restrict__ Vh, char* lds, f32x16 (&o)[4], float& l_out, const int wave_s) {
;     ...
;     const unsigned cv_ldo = (unsigned)(((tid >> 4) * 2 * 2048 + (tid & 15) * 4) * 4), cv_sto = (unsigned)((tid >> 3) * 2048 + 8 * (tid & 7));
;     const int cv_lw = OFF_CV + (4 * (tid & 15)) * 68 + 2 * (tid >> 4), cv_lr = OFF_CV + (tid >> 3) * 68 + 8 * (tid & 7);
;     f32x4 cvA = f32x4{}, cvB = f32x4{}; unsigned cvr0 = 0, cvr1 = 0;
.LBB4_795:
	s_lshl_b32 s20, s58, 8
	s_and_b32 s20, s20, 0x1f00
	s_add_u32 s24, s12, s20
	s_addc_u32 s25, s13, 0
	s_add_u32 s66, s24, 0x2000
	s_addc_u32 s67, s25, 0
	global_load_dwordx4 v[160:163], v213, s[24:25] nt
	global_load_dwordx4 v[164:167], v213, s[66:67] nt
.LBB4_796:
	v_exp_f32_e32 v182, v128
	v_exp_f32_e32 v234, v129
	v_exp_f32_e32 v235, v130
	v_exp_f32_e32 v236, v131
	v_exp_f32_e32 v237, v132
	v_exp_f32_e32 v238, v133
	v_exp_f32_e32 v239, v134
	v_exp_f32_e32 v240, v135
	v_exp_f32_e32 v241, v136
	v_exp_f32_e32 v242, v137
	v_exp_f32_e32 v243, v138
	v_exp_f32_e32 v244, v139
	v_exp_f32_e32 v245, v140
	v_exp_f32_e32 v246, v141
	v_exp_f32_e32 v247, v142
	v_exp_f32_e32 v248, v143
	v_add_u32_e32 v101, s65, v208
	v_add_u32_e32 v102, s65, v209
	v_add_u32_e32 v103, s65, v210
	ds_read_b128 v[172:175], v101 offset:49152
	ds_read_b128 v[176:179], v101 offset:53248
	ds_read_b128 v[218:221], v102 offset:49152
	ds_read_b128 v[222:225], v102 offset:53248
	ds_read_b128 v[226:229], v103 offset:49152
	ds_read_b128 v[230:233], v103 offset:53248
	v_exp_f32_e32 v112, v112
	v_exp_f32_e32 v113, v113
	v_exp_f32_e32 v114, v114
	s_waitcnt lgkmcnt(7)
	v_mfma_f32_32x32x16_bf16 v[128:143], v[96:99], v[156:159], v[80:95]
	v_exp_f32_e32 v115, v115
	v_exp_f32_e32 v116, v116
	v_exp_f32_e32 v117, v117
	v_exp_f32_e32 v118, v118
	v_exp_f32_e32 v119, v119
	s_waitcnt lgkmcnt(6)
	v_mfma_f32_32x32x16_bf16 v[96:111], v[168:171], v[156:159], v[80:95]
	v_exp_f32_e32 v168, v120
	v_add_f32_e32 v120, 0, v182
	v_add_f32_e32 v120, v234, v120
	v_add_f32_e32 v120, v235, v120
	v_add_f32_e32 v120, v236, v120
	v_add_f32_e32 v120, v237, v120
	v_add_f32_e32 v120, v238, v120
	v_add_f32_e32 v120, v239, v120
	v_add_f32_e32 v120, v240, v120
	v_add_f32_e32 v120, v241, v120
	v_add_f32_e32 v120, v242, v120
	s_waitcnt lgkmcnt(5)
	v_mfma_f32_32x32x16_bf16 v[128:143], v[172:175], v[152:155], v[128:143]
	v_add_f32_e32 v120, v243, v120
	v_add_f32_e32 v120, v244, v120
	v_add_f32_e32 v120, v245, v120
	v_add_f32_e32 v120, v246, v120
	v_add_f32_e32 v120, v247, v120
	v_add_f32_e32 v120, v248, v120
	v_add_f32_e32 v120, v112, v120
	s_waitcnt lgkmcnt(4)
	v_mfma_f32_32x32x16_bf16 v[96:111], v[176:179], v[152:155], v[96:111]
	v_add_f32_e32 v120, v113, v120
	v_add_f32_e32 v120, v114, v120
	v_add_f32_e32 v120, v115, v120
	v_add_f32_e32 v120, v116, v120
	v_exp_f32_e32 v169, v121
	v_add_f32_e32 v120, v117, v120
	v_exp_f32_e32 v170, v122
	s_waitcnt lgkmcnt(3)
	v_mfma_f32_32x32x16_bf16 v[128:143], v[218:221], v[148:151], v[128:143]
	v_add_f32_e32 v120, v118, v120
	v_exp_f32_e32 v171, v123
	v_add_f32_e32 v120, v119, v120
	v_exp_f32_e32 v172, v124
	v_add_f32_e32 v120, v168, v120
	v_exp_f32_e32 v173, v125
	v_add_f32_e32 v120, v169, v120
	s_waitcnt lgkmcnt(2)
	v_mfma_f32_32x32x16_bf16 v[96:111], v[222:225], v[148:151], v[96:111]
	v_exp_f32_e32 v174, v126
	v_add_f32_e32 v120, v170, v120
	v_exp_f32_e32 v175, v127
	v_add_f32_e32 v120, v171, v120
	v_add_f32_e32 v120, v172, v120
	v_add_f32_e32 v120, v173, v120
	v_add_f32_e32 v120, v174, v120
	s_waitcnt lgkmcnt(1)
	v_mfma_f32_32x32x16_bf16 v[128:143], v[226:229], v[144:147], v[128:143]
	v_add_f32_e32 v217, v175, v120
	v_mov_b32_e32 v218, v217
	v_cvt_pk_bf16_f32 v120, v182, v234
	v_cvt_pk_bf16_f32 v121, v235, v236
	v_cvt_pk_bf16_f32 v122, v237, v238
	v_cvt_pk_bf16_f32 v123, v239, v240
	v_cvt_pk_bf16_f32 v124, v241, v242
	s_waitcnt lgkmcnt(0)
	v_mfma_f32_32x32x16_bf16 v[96:111], v[230:233], v[144:147], v[96:111]
	v_cvt_pk_bf16_f32 v125, v243, v244
	v_cvt_pk_bf16_f32 v126, v245, v246
	v_cvt_pk_bf16_f32 v127, v247, v248
	v_cvt_pk_bf16_f32 v112, v112, v113
	v_cvt_pk_bf16_f32 v113, v114, v115
	v_cvt_pk_bf16_f32 v114, v116, v117
	v_cvt_pk_bf16_f32 v115, v118, v119
	v_cvt_pk_bf16_f32 v116, v168, v169
	v_cvt_pk_bf16_f32 v117, v170, v171
	v_cvt_pk_bf16_f32 v118, v172, v173
	v_cvt_pk_bf16_f32 v119, v174, v175
	v_permlane32_swap_b32_e32 v217, v218
	v_permlane32_swap_b32_e32 v120, v122
	v_permlane32_swap_b32_e32 v121, v123
	v_permlane32_swap_b32_e32 v124, v126
	v_permlane32_swap_b32_e32 v125, v127
	v_permlane32_swap_b32_e32 v112, v114
	v_permlane32_swap_b32_e32 v113, v115
	v_permlane32_swap_b32_e32 v116, v118
	v_permlane32_swap_b32_e32 v117, v119
	s_add_u32 s24, s34, 0x2380c000
	s_addc_u32 s25, s35, 0
	s_add_u32 s34, s34, 0x2380e000
	s_addc_u32 s35, s35, 0
	s_add_u32 s66, s37, 0x21886000
	s_addc_u32 s67, s64, 0
	global_load_dwordx4 v[176:179], v200, s[24:25]
	global_load_dwordx4 v[172:175], v200, s[34:35]
	s_nop 0
	global_load_dwordx4 v[168:171], v201, s[66:67]
	s_and_b64 vcc, exec, s[2:3]
	s_cbranch_vccnz .LBB4_798
	s_mov_b64 s[2:3], s[8:9]
	global_store_dwordx2 v193, v[184:185], s[2:3] nt

; DI void finishSM(f32x16& p0, f32x16& p1, float alpha, float& l_reg, bf16x8& pa0, bf16x8& pa1, bf16x8& pa2, bf16x8& pa3) {
; #pragma unroll
;     for (int r = 0; r < 16; ++r) p1[r] = __builtin_amdgcn_exp2f(p1[r]);
;     float ps = 0;
; #pragma unroll
;     for (int r = 0; r < 16; ++r) ps += p0[r];
; #pragma unroll
;     for (int r = 0; r < 16; ++r) ps += p1[r];
;     { auto rr = __builtin_amdgcn_permlane32_swap(__float_as_uint(ps), __float_as_uint(ps), false, false); ps = __uint_as_float(rr[0]) + __uint_as_float(rr[1]); }
;     l_reg = l_reg * alpha + ps;
;     ...
;     AT_PK4(p0, 0, pa0); AT_PK4(p0, 8, pa1); AT_PK4(p1, 0, pa2); AT_PK4(p1, 8, pa3);
;     ...
; }
; DI void qkt(f32x16& p0, f32x16& p1, const char* Ks, const bf16x8* qr, const f32x16& negm, int r32, int hi) {
; #pragma unroll
;     for (int d0 = 0; d0 < 4; ++d0) { const int cb = (d0 * 16 + hi * 8) * 2;
;         const bf16x8 b0 = *reinterpret_cast<const bf16x8*>(Ks + AT_KSWZ(r32, cb));
;         const bf16x8 b1 = *reinterpret_cast<const bf16x8*>(Ks + AT_KSWZ(32 + r32, cb));
;         p0 = __builtin_amdgcn_mfma_f32_32x32x16_bf16(b0, qr[d0], d0 == 0 ? negm : p0, 0, 0, 0);
;         p1 = __builtin_amdgcn_mfma_f32_32x32x16_bf16(b1, qr[d0], d0 == 0 ? negm : p1, 0, 0, 0); }
; DI void attn_pass(const Frame& F, CvRide& cv, const bf16_t* __restrict__ Qb, const bf16_t* __restrict__ Kh, const bf16_t* __restrict__ Vh, char* lds, f32x16 (&o)[4], float& l_out, const int wave_s) {
;     ...
;     const unsigned cv_ldo = (unsigned)(((tid >> 4) * 2 * 2048 + (tid & 15) * 4) * 4), cv_sto = (unsigned)((tid >> 3) * 2048 + 8 * (tid & 7));
;     const int cv_lw = OFF_CV + (4 * (tid & 15)) * 68 + 2 * (tid >> 4), cv_lr = OFF_CV + (tid >> 3) * 68 + 8 * (tid & 7);
;     f32x4 cvA = f32x4{}, cvB = f32x4{}; unsigned cvr0 = 0, cvr1 = 0;
.LBB4_848:
	s_lshl_b32 s26, s58, 8
	s_and_b32 s26, s26, 0x1f00
	s_add_u32 s34, s12, s26
	s_addc_u32 s35, s13, 0
	s_add_u32 s66, s34, 0x2000
	s_addc_u32 s67, s35, 0
	global_load_dwordx4 v[160:163], v209, s[34:35] nt
	global_load_dwordx4 v[164:167], v209, s[66:67] nt
.LBB4_849:
	s_lshl_b32 s26, s64, 13
	s_add_i32 s26, s26, 0
	v_add_u32_e32 v72, s26, v204
	v_add_u32_e32 v112, s26, v205
	v_add_u32_e32 v180, s26, v206
	s_waitcnt lgkmcnt(1)
	v_mfma_f32_32x32x16_bf16 v[128:143], v[64:67], v[156:159], v[80:95]
	ds_read_b128 v[64:67], v72 offset:49152
	ds_read_b128 v[72:75], v72 offset:53248
	ds_read_b128 v[76:79], v112 offset:49152
	ds_read_b128 v[220:223], v112 offset:53248
	v_exp_f32_e32 v182, v97
	v_exp_f32_e32 v213, v98
	v_exp_f32_e32 v214, v99
	v_exp_f32_e32 v219, v100
	v_exp_f32_e32 v228, v101
	s_waitcnt lgkmcnt(4)
	v_mfma_f32_32x32x16_bf16 v[112:127], v[68:71], v[156:159], v[80:95]
	ds_read_b128 v[68:71], v180 offset:49152
	ds_read_b128 v[224:227], v180 offset:53248
	v_exp_f32_e32 v180, v96
	v_cvt_pk_bf16_f32 v96, v216, v218
	v_cvt_pk_bf16_f32 v97, v179, v217
	v_cvt_pk_bf16_f32 v98, v177, v215
	v_cvt_pk_bf16_f32 v99, v176, v178
	s_waitcnt lgkmcnt(4)
	v_mfma_f32_32x32x16_bf16 v[112:127], v[72:75], v[152:155], v[112:127]
	v_add_f32_e32 v75, 0, v216
	v_add_f32_e32 v75, v218, v75
	v_add_f32_e32 v75, v179, v75
	v_add_f32_e32 v75, v217, v75
	v_add_f32_e32 v75, v177, v75
	v_add_f32_e32 v75, v215, v75
	v_add_f32_e32 v75, v176, v75
	v_mfma_f32_32x32x16_bf16 v[128:143], v[64:67], v[152:155], v[128:143]
	v_add_f32_e32 v75, v178, v75
	v_add_f32_e32 v75, v173, v75
	v_add_f32_e32 v75, v175, v75
	v_add_f32_e32 v75, v171, v75
	v_add_f32_e32 v75, v174, v75
	v_add_f32_e32 v75, v169, v75
	v_add_f32_e32 v75, v172, v75
	s_waitcnt lgkmcnt(3)
	v_mfma_f32_32x32x16_bf16 v[128:143], v[76:79], v[148:151], v[128:143]
	v_add_f32_e32 v75, v168, v75
	v_add_f32_e32 v75, v170, v75
	v_add_f32_e32 v75, v180, v75
	v_add_f32_e32 v75, v182, v75
	v_exp_f32_e32 v64, v102
	v_exp_f32_e32 v65, v103
	v_exp_f32_e32 v66, v104
	s_waitcnt lgkmcnt(2)
	v_mfma_f32_32x32x16_bf16 v[112:127], v[220:223], v[148:151], v[112:127]
	v_exp_f32_e32 v67, v105
	v_exp_f32_e32 v105, v106
	v_exp_f32_e32 v106, v107
	v_exp_f32_e32 v107, v108
	v_exp_f32_e32 v72, v109
	v_exp_f32_e32 v73, v110
	v_exp_f32_e32 v74, v111
	s_waitcnt lgkmcnt(1)
	v_mfma_f32_32x32x16_bf16 v[128:143], v[68:71], v[144:147], v[128:143]
	v_add_f32_e32 v68, v213, v75
	v_add_f32_e32 v68, v214, v68
	v_add_f32_e32 v68, v219, v68
	v_add_f32_e32 v68, v228, v68
	v_add_f32_e32 v68, v64, v68
	v_add_f32_e32 v68, v65, v68
	v_add_f32_e32 v68, v66, v68
	v_add_f32_e32 v68, v67, v68
	s_waitcnt lgkmcnt(0)
	v_mfma_f32_32x32x16_bf16 v[112:127], v[224:227], v[144:147], v[112:127]
	v_add_f32_e32 v68, v105, v68
	v_add_f32_e32 v68, v106, v68
	v_add_f32_e32 v68, v107, v68
	v_add_f32_e32 v68, v72, v68
	v_add_f32_e32 v68, v73, v68
	v_add_f32_e32 v211, v74, v68
	v_mov_b32_e32 v212, v211
	v_cvt_pk_bf16_f32 v108, v173, v175
	v_cvt_pk_bf16_f32 v109, v171, v174
	v_cvt_pk_bf16_f32 v110, v169, v172
	v_cvt_pk_bf16_f32 v111, v168, v170
	v_cvt_pk_bf16_f32 v100, v180, v182
	v_cvt_pk_bf16_f32 v101, v213, v214
	v_cvt_pk_bf16_f32 v102, v219, v228
	v_cvt_pk_bf16_f32 v103, v64, v65
	v_cvt_pk_bf16_f32 v104, v66, v67
	v_cvt_pk_bf16_f32 v105, v105, v106
	v_cvt_pk_bf16_f32 v106, v107, v72
	v_cvt_pk_bf16_f32 v107, v73, v74
	s_nop 1
	v_permlane32_swap_b32_e32 v211, v212
	v_permlane32_swap_b32_e32 v96, v98
	v_permlane32_swap_b32_e32 v97, v99
	v_permlane32_swap_b32_e32 v108, v110
	v_permlane32_swap_b32_e32 v109, v111
	v_permlane32_swap_b32_e32 v100, v102
	v_permlane32_swap_b32_e32 v101, v103
	v_permlane32_swap_b32_e32 v104, v106
	v_permlane32_swap_b32_e32 v105, v107
	s_add_u32 s66, s46, s28
	s_addc_u32 s67, s47, s29
	s_add_u32 s34, s66, 0x23808000
	s_addc_u32 s35, s67, 0
	s_add_u32 s76, s66, 0x2380a000
	s_addc_u32 s77, s67, 0
	s_add_u32 s74, s46, s24
	s_addc_u32 s75, s47, s25
	s_add_u32 s78, s74, 0x21804000
	s_addc_u32 s79, s75, 0
	global_load_dwordx4 v[176:179], v196, s[34:35]
	global_load_dwordx4 v[172:175], v196, s[76:77]
	global_load_dwordx4 v[168:171], v197, s[78:79]
	s_andn2_b64 vcc, exec, s[2:3]
	s_cbranch_vccnz .LBB4_851
	s_mov_b64 s[2:3], s[8:9]
	global_store_dwordx2 v188, v[184:185], s[2:3] nt

; DI void finishSM(f32x16& p0, f32x16& p1, float alpha, float& l_reg, bf16x8& pa0, bf16x8& pa1, bf16x8& pa2, bf16x8& pa3) {
; #pragma unroll
;     for (int r = 0; r < 16; ++r) p1[r] = __builtin_amdgcn_exp2f(p1[r]);
;     float ps = 0;
; #pragma unroll
;     for (int r = 0; r < 16; ++r) ps += p0[r];
; #pragma unroll
;     for (int r = 0; r < 16; ++r) ps += p1[r];
;     { auto rr = __builtin_amdgcn_permlane32_swap(__float_as_uint(ps), __float_as_uint(ps), false, false); ps = __uint_as_float(rr[0]) + __uint_as_float(rr[1]); }
;     l_reg = l_reg * alpha + ps;
;     ...
;     AT_PK4(p0, 0, pa0); AT_PK4(p0, 8, pa1); AT_PK4(p1, 0, pa2); AT_PK4(p1, 8, pa3);
;     ...
; }
; DI void qkt(f32x16& p0, f32x16& p1, const char* Ks, const bf16x8* qr, const f32x16& negm, int r32, int hi) {
; #pragma unroll
;     for (int d0 = 0; d0 < 4; ++d0) { const int cb = (d0 * 16 + hi * 8) * 2;
;         const bf16x8 b0 = *reinterpret_cast<const bf16x8*>(Ks + AT_KSWZ(r32, cb));
;         const bf16x8 b1 = *reinterpret_cast<const bf16x8*>(Ks + AT_KSWZ(32 + r32, cb));
;         p0 = __builtin_amdgcn_mfma_f32_32x32x16_bf16(b0, qr[d0], d0 == 0 ? negm : p0, 0, 0, 0);
;         p1 = __builtin_amdgcn_mfma_f32_32x32x16_bf16(b1, qr[d0], d0 == 0 ? negm : p1, 0, 0, 0); }
; DI void attn_pass(const Frame& F, CvRide& cv, const bf16_t* __restrict__ Qb, const bf16_t* __restrict__ Kh, const bf16_t* __restrict__ Vh, char* lds, f32x16 (&o)[4], float& l_out, const int wave_s) {
;     ...
;     const unsigned cv_ldo = (unsigned)(((tid >> 4) * 2 * 2048 + (tid & 15) * 4) * 4), cv_sto = (unsigned)((tid >> 3) * 2048 + 8 * (tid & 7));
;     const int cv_lw = OFF_CV + (4 * (tid & 15)) * 68 + 2 * (tid >> 4), cv_lr = OFF_CV + (tid >> 3) * 68 + 8 * (tid & 7);
;     f32x4 cvA = f32x4{}, cvB = f32x4{}; unsigned cvr0 = 0, cvr1 = 0;
.LBB4_869:
	s_lshl_b32 s26, s58, 8
	s_and_b32 s26, s26, 0x1f00
	s_add_u32 s34, s12, s26
	s_addc_u32 s35, s13, 0
	s_add_u32 s78, s34, 0x2000
	s_addc_u32 s79, s35, 0
	global_load_dwordx4 v[160:163], v209, s[34:35] nt
	global_load_dwordx4 v[164:167], v209, s[78:79] nt
.LBB4_870:
	v_exp_f32_e32 v182, v128
	v_exp_f32_e32 v230, v129
	v_exp_f32_e32 v231, v130
	v_exp_f32_e32 v232, v131
	v_exp_f32_e32 v233, v132
	v_exp_f32_e32 v234, v133
	v_exp_f32_e32 v235, v134
	v_exp_f32_e32 v236, v135
	v_exp_f32_e32 v237, v136
	v_exp_f32_e32 v238, v137
	v_exp_f32_e32 v239, v138
	v_exp_f32_e32 v240, v139
	v_exp_f32_e32 v241, v140
	v_exp_f32_e32 v242, v141
	v_exp_f32_e32 v243, v142
	v_exp_f32_e32 v244, v143
	v_add_u32_e32 v101, s76, v204
	v_add_u32_e32 v102, s76, v205
	v_add_u32_e32 v103, s76, v206
	ds_read_b128 v[172:175], v101 offset:49152
	ds_read_b128 v[176:179], v101 offset:53248
	ds_read_b128 v[214:217], v102 offset:49152
	ds_read_b128 v[218:221], v102 offset:53248
	ds_read_b128 v[222:225], v103 offset:49152
	ds_read_b128 v[226:229], v103 offset:53248
	v_exp_f32_e32 v112, v112
	v_exp_f32_e32 v113, v113
	v_exp_f32_e32 v114, v114
	s_waitcnt lgkmcnt(7)
	v_mfma_f32_32x32x16_bf16 v[128:143], v[96:99], v[156:159], v[80:95]
	v_exp_f32_e32 v115, v115
	v_exp_f32_e32 v116, v116
	v_exp_f32_e32 v117, v117
	v_exp_f32_e32 v118, v118
	v_exp_f32_e32 v119, v119
	s_waitcnt lgkmcnt(6)
	v_mfma_f32_32x32x16_bf16 v[96:111], v[168:171], v[156:159], v[80:95]
	v_exp_f32_e32 v168, v120
	v_add_f32_e32 v120, 0, v182
	v_add_f32_e32 v120, v230, v120
	v_add_f32_e32 v120, v231, v120
	v_add_f32_e32 v120, v232, v120
	v_add_f32_e32 v120, v233, v120
	v_add_f32_e32 v120, v234, v120
	v_add_f32_e32 v120, v235, v120
	v_add_f32_e32 v120, v236, v120
	v_add_f32_e32 v120, v237, v120
	v_add_f32_e32 v120, v238, v120
	s_waitcnt lgkmcnt(5)
	v_mfma_f32_32x32x16_bf16 v[128:143], v[172:175], v[152:155], v[128:143]
	v_add_f32_e32 v120, v239, v120
	v_add_f32_e32 v120, v240, v120
	v_add_f32_e32 v120, v241, v120
	v_add_f32_e32 v120, v242, v120
	v_add_f32_e32 v120, v243, v120
	v_add_f32_e32 v120, v244, v120
	v_add_f32_e32 v120, v112, v120
	s_waitcnt lgkmcnt(4)
	v_mfma_f32_32x32x16_bf16 v[96:111], v[176:179], v[152:155], v[96:111]
	v_add_f32_e32 v120, v113, v120
	v_add_f32_e32 v120, v114, v120
	v_add_f32_e32 v120, v115, v120
	v_add_f32_e32 v120, v116, v120
	v_exp_f32_e32 v169, v121
	v_add_f32_e32 v120, v117, v120
	v_exp_f32_e32 v170, v122
	s_waitcnt lgkmcnt(3)
	v_mfma_f32_32x32x16_bf16 v[128:143], v[214:217], v[148:151], v[128:143]
	v_add_f32_e32 v120, v118, v120
	v_exp_f32_e32 v171, v123
	v_add_f32_e32 v120, v119, v120
	v_exp_f32_e32 v172, v124
	v_add_f32_e32 v120, v168, v120
	v_exp_f32_e32 v173, v125
	v_add_f32_e32 v120, v169, v120
	s_waitcnt lgkmcnt(2)
	v_mfma_f32_32x32x16_bf16 v[96:111], v[218:221], v[148:151], v[96:111]
	v_exp_f32_e32 v174, v126
	v_add_f32_e32 v120, v170, v120
	v_exp_f32_e32 v175, v127
	v_add_f32_e32 v120, v171, v120
	v_add_f32_e32 v120, v172, v120
	v_add_f32_e32 v120, v173, v120
	v_add_f32_e32 v120, v174, v120
	s_waitcnt lgkmcnt(1)
	v_mfma_f32_32x32x16_bf16 v[128:143], v[222:225], v[144:147], v[128:143]
	v_add_f32_e32 v213, v175, v120
	v_mov_b32_e32 v214, v213
	v_cvt_pk_bf16_f32 v120, v182, v230
	v_cvt_pk_bf16_f32 v121, v231, v232
	v_cvt_pk_bf16_f32 v122, v233, v234
	v_cvt_pk_bf16_f32 v123, v235, v236
	v_cvt_pk_bf16_f32 v124, v237, v238
	s_waitcnt lgkmcnt(0)
	v_mfma_f32_32x32x16_bf16 v[96:111], v[226:229], v[144:147], v[96:111]
	v_cvt_pk_bf16_f32 v125, v239, v240
	v_cvt_pk_bf16_f32 v126, v241, v242
	v_cvt_pk_bf16_f32 v127, v243, v244
	v_cvt_pk_bf16_f32 v112, v112, v113
	v_cvt_pk_bf16_f32 v113, v114, v115
	v_cvt_pk_bf16_f32 v114, v116, v117
	v_cvt_pk_bf16_f32 v115, v118, v119
	v_cvt_pk_bf16_f32 v116, v168, v169
	v_cvt_pk_bf16_f32 v117, v170, v171
	v_cvt_pk_bf16_f32 v118, v172, v173
	v_cvt_pk_bf16_f32 v119, v174, v175
	v_permlane32_swap_b32_e32 v213, v214
	v_permlane32_swap_b32_e32 v120, v122
	v_permlane32_swap_b32_e32 v121, v123
	v_permlane32_swap_b32_e32 v124, v126
	v_permlane32_swap_b32_e32 v125, v127
	v_permlane32_swap_b32_e32 v112, v114
	v_permlane32_swap_b32_e32 v113, v115
	v_permlane32_swap_b32_e32 v116, v118
	v_permlane32_swap_b32_e32 v117, v119
	s_add_u32 s34, s66, 0x2380c000
	s_addc_u32 s35, s67, 0
	s_add_u32 s66, s66, 0x2380e000
	s_addc_u32 s67, s67, 0
	s_add_u32 s74, s74, 0x21806000
	s_addc_u32 s75, s75, 0
	global_load_dwordx4 v[176:179], v196, s[34:35]
	global_load_dwordx4 v[172:175], v196, s[66:67]
	s_nop 0
	global_load_dwordx4 v[168:171], v197, s[74:75]
	s_and_b64 vcc, exec, s[2:3]
	s_cbranch_vccnz .LBB4_872
	s_mov_b64 s[2:3], s[8:9]
	global_store_dwordx2 v188, v[184:185], s[2:3] nt

; DI void finishSM(f32x16& p0, f32x16& p1, float alpha, float& l_reg, bf16x8& pa0, bf16x8& pa1, bf16x8& pa2, bf16x8& pa3) {
; #pragma unroll
;     for (int r = 0; r < 16; ++r) p1[r] = __builtin_amdgcn_exp2f(p1[r]);
;     float ps = 0;
; #pragma unroll
;     for (int r = 0; r < 16; ++r) ps += p0[r];
; #pragma unroll
;     for (int r = 0; r < 16; ++r) ps += p1[r];
;     { auto rr = __builtin_amdgcn_permlane32_swap(__float_as_uint(ps), __float_as_uint(ps), false, false); ps = __uint_as_float(rr[0]) + __uint_as_float(rr[1]); }
;     l_reg = l_reg * alpha + ps;
;     ...
;     AT_PK4(p0, 0, pa0); AT_PK4(p0, 8, pa1); AT_PK4(p1, 0, pa2); AT_PK4(p1, 8, pa3);
;     ...
; }
; DI void qkt(f32x16& p0, f32x16& p1, const char* Ks, const bf16x8* qr, const f32x16& negm, int r32, int hi) {
; #pragma unroll
;     for (int d0 = 0; d0 < 4; ++d0) { const int cb = (d0 * 16 + hi * 8) * 2;
;         const bf16x8 b0 = *reinterpret_cast<const bf16x8*>(Ks + AT_KSWZ(r32, cb));
;         const bf16x8 b1 = *reinterpret_cast<const bf16x8*>(Ks + AT_KSWZ(32 + r32, cb));
;         p0 = __builtin_amdgcn_mfma_f32_32x32x16_bf16(b0, qr[d0], d0 == 0 ? negm : p0, 0, 0, 0);
;         p1 = __builtin_amdgcn_mfma_f32_32x32x16_bf16(b1, qr[d0], d0 == 0 ? negm : p1, 0, 0, 0); }
; DI void attn_pass(const Frame& F, CvRide& cv, const bf16_t* __restrict__ Qb, const bf16_t* __restrict__ Kh, const bf16_t* __restrict__ Vh, char* lds, f32x16 (&o)[4], float& l_out, const int wave_s) {
;     ...
;     const unsigned cv_ldo = (unsigned)(((tid >> 4) * 2 * 2048 + (tid & 15) * 4) * 4), cv_sto = (unsigned)((tid >> 3) * 2048 + 8 * (tid & 7));
;     const int cv_lw = OFF_CV + (4 * (tid & 15)) * 68 + 2 * (tid >> 4), cv_lr = OFF_CV + (tid >> 3) * 68 + 8 * (tid & 7);
;     f32x4 cvA = f32x4{}, cvB = f32x4{}; unsigned cvr0 = 0, cvr1 = 0;
.LBB4_922:
	s_lshl_b32 s18, s58, 8
	s_and_b32 s18, s18, 0x1f00
	s_add_u32 s24, s12, s18
	s_addc_u32 s25, s13, 0
	s_add_u32 s34, s24, 0x2000
	s_addc_u32 s35, s25, 0
	global_load_dwordx4 v[160:163], v213, s[24:25] nt
	global_load_dwordx4 v[164:167], v213, s[34:35] nt
.LBB4_923:
	s_lshl_b32 s18, s30, 13
	s_add_i32 s18, s18, 0
	v_add_u32_e32 v72, s18, v208
	v_add_u32_e32 v112, s18, v209
	v_add_u32_e32 v180, s18, v210
	s_waitcnt lgkmcnt(1)
	v_mfma_f32_32x32x16_bf16 v[128:143], v[64:67], v[156:159], v[80:95]
	ds_read_b128 v[64:67], v72 offset:49152
	ds_read_b128 v[72:75], v72 offset:53248
	ds_read_b128 v[76:79], v112 offset:49152
	ds_read_b128 v[224:227], v112 offset:53248
	v_exp_f32_e32 v182, v97
	v_exp_f32_e32 v217, v98
	v_exp_f32_e32 v218, v99
	v_exp_f32_e32 v223, v100
	v_exp_f32_e32 v232, v101
	s_waitcnt lgkmcnt(4)
	v_mfma_f32_32x32x16_bf16 v[112:127], v[68:71], v[156:159], v[80:95]
	ds_read_b128 v[68:71], v180 offset:49152
	ds_read_b128 v[228:231], v180 offset:53248
	v_exp_f32_e32 v180, v96
	v_cvt_pk_bf16_f32 v96, v220, v222
	v_cvt_pk_bf16_f32 v97, v179, v221
	v_cvt_pk_bf16_f32 v98, v177, v219
	v_cvt_pk_bf16_f32 v99, v176, v178
	s_waitcnt lgkmcnt(4)
	v_mfma_f32_32x32x16_bf16 v[112:127], v[72:75], v[152:155], v[112:127]
	v_add_f32_e32 v75, 0, v220
	v_add_f32_e32 v75, v222, v75
	v_add_f32_e32 v75, v179, v75
	v_add_f32_e32 v75, v221, v75
	v_add_f32_e32 v75, v177, v75
	v_add_f32_e32 v75, v219, v75
	v_add_f32_e32 v75, v176, v75
	v_mfma_f32_32x32x16_bf16 v[128:143], v[64:67], v[152:155], v[128:143]
	v_add_f32_e32 v75, v178, v75
	v_add_f32_e32 v75, v173, v75
	v_add_f32_e32 v75, v175, v75
	v_add_f32_e32 v75, v171, v75
	v_add_f32_e32 v75, v174, v75
	v_add_f32_e32 v75, v169, v75
	v_add_f32_e32 v75, v172, v75
	s_waitcnt lgkmcnt(3)
	v_mfma_f32_32x32x16_bf16 v[128:143], v[76:79], v[148:151], v[128:143]
	v_add_f32_e32 v75, v168, v75
	v_add_f32_e32 v75, v170, v75
	v_add_f32_e32 v75, v180, v75
	v_add_f32_e32 v75, v182, v75
	v_exp_f32_e32 v64, v102
	v_exp_f32_e32 v65, v103
	v_exp_f32_e32 v66, v104
	s_waitcnt lgkmcnt(2)
	v_mfma_f32_32x32x16_bf16 v[112:127], v[224:227], v[148:151], v[112:127]
	v_exp_f32_e32 v67, v105
	v_exp_f32_e32 v105, v106
	v_exp_f32_e32 v106, v107
	v_exp_f32_e32 v107, v108
	v_exp_f32_e32 v72, v109
	v_exp_f32_e32 v73, v110
	v_exp_f32_e32 v74, v111
	s_waitcnt lgkmcnt(1)
	v_mfma_f32_32x32x16_bf16 v[128:143], v[68:71], v[144:147], v[128:143]
	v_add_f32_e32 v68, v217, v75
	v_add_f32_e32 v68, v218, v68
	v_add_f32_e32 v68, v223, v68
	v_add_f32_e32 v68, v232, v68
	v_add_f32_e32 v68, v64, v68
	v_add_f32_e32 v68, v65, v68
	v_add_f32_e32 v68, v66, v68
	v_add_f32_e32 v68, v67, v68
	s_waitcnt lgkmcnt(0)
	v_mfma_f32_32x32x16_bf16 v[112:127], v[228:231], v[144:147], v[112:127]
	v_add_f32_e32 v68, v105, v68
	v_add_f32_e32 v68, v106, v68
	v_add_f32_e32 v68, v107, v68
	v_add_f32_e32 v68, v72, v68
	v_add_f32_e32 v68, v73, v68
	v_add_f32_e32 v215, v74, v68
	v_mov_b32_e32 v216, v215
	v_cvt_pk_bf16_f32 v108, v173, v175
	v_cvt_pk_bf16_f32 v109, v171, v174
	v_cvt_pk_bf16_f32 v110, v169, v172
	v_cvt_pk_bf16_f32 v111, v168, v170
	v_cvt_pk_bf16_f32 v100, v180, v182
	v_cvt_pk_bf16_f32 v101, v217, v218
	v_cvt_pk_bf16_f32 v102, v223, v232
	v_cvt_pk_bf16_f32 v103, v64, v65
	v_cvt_pk_bf16_f32 v104, v66, v67
	v_cvt_pk_bf16_f32 v105, v105, v106
	v_cvt_pk_bf16_f32 v106, v107, v72
	v_cvt_pk_bf16_f32 v107, v73, v74
	s_nop 1
	v_permlane32_swap_b32_e32 v215, v216
	v_permlane32_swap_b32_e32 v96, v98
	v_permlane32_swap_b32_e32 v97, v99
	v_permlane32_swap_b32_e32 v108, v110
	v_permlane32_swap_b32_e32 v109, v111
	v_permlane32_swap_b32_e32 v100, v102
	v_permlane32_swap_b32_e32 v101, v103
	v_permlane32_swap_b32_e32 v104, v106
	v_permlane32_swap_b32_e32 v105, v107
	s_add_u32 s34, s46, s16
	s_addc_u32 s35, s47, s17
	s_add_u32 s24, s34, 0x23808000
	s_addc_u32 s25, s35, 0
	s_add_u32 s54, s34, 0x2380a000
	s_addc_u32 s55, s35, 0
	s_add_u32 s42, s46, s20
	s_addc_u32 s43, s47, s21
	s_add_u32 s56, s42, 0x21884000
	s_addc_u32 s57, s43, 0
	global_load_dwordx4 v[176:179], v200, s[24:25]
	global_load_dwordx4 v[172:175], v200, s[54:55]
	global_load_dwordx4 v[168:171], v201, s[56:57]
	s_andn2_b64 vcc, exec, s[2:3]
	s_cbranch_vccnz .LBB4_925
	s_mov_b64 s[2:3], s[8:9]
	global_store_dwordx2 v193, v[184:185], s[2:3] nt

; DI void finishSM(f32x16& p0, f32x16& p1, float alpha, float& l_reg, bf16x8& pa0, bf16x8& pa1, bf16x8& pa2, bf16x8& pa3) {
; #pragma unroll
;     for (int r = 0; r < 16; ++r) p1[r] = __builtin_amdgcn_exp2f(p1[r]);
;     float ps = 0;
; #pragma unroll
;     for (int r = 0; r < 16; ++r) ps += p0[r];
; #pragma unroll
;     for (int r = 0; r < 16; ++r) ps += p1[r];
;     { auto rr = __builtin_amdgcn_permlane32_swap(__float_as_uint(ps), __float_as_uint(ps), false, false); ps = __uint_as_float(rr[0]) + __uint_as_float(rr[1]); }
;     l_reg = l_reg * alpha + ps;
;     ...
;     AT_PK4(p0, 0, pa0); AT_PK4(p0, 8, pa1); AT_PK4(p1, 0, pa2); AT_PK4(p1, 8, pa3);
;     ...
; }
; DI void qkt(f32x16& p0, f32x16& p1, const char* Ks, const bf16x8* qr, const f32x16& negm, int r32, int hi) {
; #pragma unroll
;     for (int d0 = 0; d0 < 4; ++d0) { const int cb = (d0 * 16 + hi * 8) * 2;
;         const bf16x8 b0 = *reinterpret_cast<const bf16x8*>(Ks + AT_KSWZ(r32, cb));
;         const bf16x8 b1 = *reinterpret_cast<const bf16x8*>(Ks + AT_KSWZ(32 + r32, cb));
;         p0 = __builtin_amdgcn_mfma_f32_32x32x16_bf16(b0, qr[d0], d0 == 0 ? negm : p0, 0, 0, 0);
;         p1 = __builtin_amdgcn_mfma_f32_32x32x16_bf16(b1, qr[d0], d0 == 0 ? negm : p1, 0, 0, 0); }
; DI void attn_pass(const Frame& F, CvRide& cv, const bf16_t* __restrict__ Qb, const bf16_t* __restrict__ Kh, const bf16_t* __restrict__ Vh, char* lds, f32x16 (&o)[4], float& l_out, const int wave_s) {
;     ...
;     const unsigned cv_ldo = (unsigned)(((tid >> 4) * 2 * 2048 + (tid & 15) * 4) * 4), cv_sto = (unsigned)((tid >> 3) * 2048 + 8 * (tid & 7));
;     const int cv_lw = OFF_CV + (4 * (tid & 15)) * 68 + 2 * (tid >> 4), cv_lr = OFF_CV + (tid >> 3) * 68 + 8 * (tid & 7);
;     f32x4 cvA = f32x4{}, cvB = f32x4{}; unsigned cvr0 = 0, cvr1 = 0;
.LBB4_943:
	s_lshl_b32 s18, s58, 8
	s_and_b32 s18, s18, 0x1f00
	s_add_u32 s24, s12, s18
	s_addc_u32 s25, s13, 0
	s_add_u32 s56, s24, 0x2000
	s_addc_u32 s57, s25, 0
	global_load_dwordx4 v[160:163], v213, s[24:25] nt
	global_load_dwordx4 v[164:167], v213, s[56:57] nt
.LBB4_944:
	v_exp_f32_e32 v182, v128
	v_exp_f32_e32 v234, v129
	v_exp_f32_e32 v235, v130
	v_exp_f32_e32 v236, v131
	v_exp_f32_e32 v237, v132
	v_exp_f32_e32 v238, v133
	v_exp_f32_e32 v239, v134
	v_exp_f32_e32 v240, v135
	v_exp_f32_e32 v241, v136
	v_exp_f32_e32 v242, v137
	v_exp_f32_e32 v243, v138
	v_exp_f32_e32 v244, v139
	v_exp_f32_e32 v245, v140
	v_exp_f32_e32 v246, v141
	v_exp_f32_e32 v247, v142
	v_exp_f32_e32 v248, v143
	v_add_u32_e32 v101, s54, v208
	v_add_u32_e32 v102, s54, v209
	v_add_u32_e32 v103, s54, v210
	ds_read_b128 v[172:175], v101 offset:49152
	ds_read_b128 v[176:179], v101 offset:53248
	ds_read_b128 v[218:221], v102 offset:49152
	ds_read_b128 v[222:225], v102 offset:53248
	ds_read_b128 v[226:229], v103 offset:49152
	ds_read_b128 v[230:233], v103 offset:53248
	v_exp_f32_e32 v112, v112
	v_exp_f32_e32 v113, v113
	v_exp_f32_e32 v114, v114
	s_waitcnt lgkmcnt(7)
	v_mfma_f32_32x32x16_bf16 v[128:143], v[96:99], v[156:159], v[80:95]
	v_exp_f32_e32 v115, v115
	v_exp_f32_e32 v116, v116
	v_exp_f32_e32 v117, v117
	v_exp_f32_e32 v118, v118
	v_exp_f32_e32 v119, v119
	s_waitcnt lgkmcnt(6)
	v_mfma_f32_32x32x16_bf16 v[96:111], v[168:171], v[156:159], v[80:95]
	v_exp_f32_e32 v168, v120
	v_add_f32_e32 v120, 0, v182
	v_add_f32_e32 v120, v234, v120
	v_add_f32_e32 v120, v235, v120
	v_add_f32_e32 v120, v236, v120
	v_add_f32_e32 v120, v237, v120
	v_add_f32_e32 v120, v238, v120
	v_add_f32_e32 v120, v239, v120
	v_add_f32_e32 v120, v240, v120
	v_add_f32_e32 v120, v241, v120
	v_add_f32_e32 v120, v242, v120
	s_waitcnt lgkmcnt(5)
	v_mfma_f32_32x32x16_bf16 v[128:143], v[172:175], v[152:155], v[128:143]
	v_add_f32_e32 v120, v243, v120
	v_add_f32_e32 v120, v244, v120
	v_add_f32_e32 v120, v245, v120
	v_add_f32_e32 v120, v246, v120
	v_add_f32_e32 v120, v247, v120
	v_add_f32_e32 v120, v248, v120
	v_add_f32_e32 v120, v112, v120
	s_waitcnt lgkmcnt(4)
	v_mfma_f32_32x32x16_bf16 v[96:111], v[176:179], v[152:155], v[96:111]
	v_add_f32_e32 v120, v113, v120
	v_add_f32_e32 v120, v114, v120
	v_add_f32_e32 v120, v115, v120
	v_add_f32_e32 v120, v116, v120
	v_exp_f32_e32 v169, v121
	v_add_f32_e32 v120, v117, v120
	v_exp_f32_e32 v170, v122
	s_waitcnt lgkmcnt(3)
	v_mfma_f32_32x32x16_bf16 v[128:143], v[218:221], v[148:151], v[128:143]
	v_add_f32_e32 v120, v118, v120
	v_exp_f32_e32 v171, v123
	v_add_f32_e32 v120, v119, v120
	v_exp_f32_e32 v172, v124
	v_add_f32_e32 v120, v168, v120
	v_exp_f32_e32 v173, v125
	v_add_f32_e32 v120, v169, v120
	s_waitcnt lgkmcnt(2)
	v_mfma_f32_32x32x16_bf16 v[96:111], v[222:225], v[148:151], v[96:111]
	v_exp_f32_e32 v174, v126
	v_add_f32_e32 v120, v170, v120
	v_exp_f32_e32 v175, v127
	v_add_f32_e32 v120, v171, v120
	v_add_f32_e32 v120, v172, v120
	v_add_f32_e32 v120, v173, v120
	v_add_f32_e32 v120, v174, v120
	s_waitcnt lgkmcnt(1)
	v_mfma_f32_32x32x16_bf16 v[128:143], v[226:229], v[144:147], v[128:143]
	v_add_f32_e32 v217, v175, v120
	v_mov_b32_e32 v218, v217
	v_cvt_pk_bf16_f32 v120, v182, v234
	v_cvt_pk_bf16_f32 v121, v235, v236
	v_cvt_pk_bf16_f32 v122, v237, v238
	v_cvt_pk_bf16_f32 v123, v239, v240
	v_cvt_pk_bf16_f32 v124, v241, v242
	s_waitcnt lgkmcnt(0)
	v_mfma_f32_32x32x16_bf16 v[96:111], v[230:233], v[144:147], v[96:111]
	v_cvt_pk_bf16_f32 v125, v243, v244
	v_cvt_pk_bf16_f32 v126, v245, v246
	v_cvt_pk_bf16_f32 v127, v247, v248
	v_cvt_pk_bf16_f32 v112, v112, v113
	v_cvt_pk_bf16_f32 v113, v114, v115
	v_cvt_pk_bf16_f32 v114, v116, v117
	v_cvt_pk_bf16_f32 v115, v118, v119
	v_cvt_pk_bf16_f32 v116, v168, v169
	v_cvt_pk_bf16_f32 v117, v170, v171
	v_cvt_pk_bf16_f32 v118, v172, v173
	v_cvt_pk_bf16_f32 v119, v174, v175
	v_permlane32_swap_b32_e32 v217, v218
	v_permlane32_swap_b32_e32 v120, v122
	v_permlane32_swap_b32_e32 v121, v123
	v_permlane32_swap_b32_e32 v124, v126
	v_permlane32_swap_b32_e32 v125, v127
	v_permlane32_swap_b32_e32 v112, v114
	v_permlane32_swap_b32_e32 v113, v115
	v_permlane32_swap_b32_e32 v116, v118
	v_permlane32_swap_b32_e32 v117, v119
	s_add_u32 s24, s34, 0x2380c000
	s_addc_u32 s25, s35, 0
	s_add_u32 s34, s34, 0x2380e000
	s_addc_u32 s35, s35, 0
	s_add_u32 s42, s42, 0x21886000
	s_addc_u32 s43, s43, 0
	global_load_dwordx4 v[176:179], v200, s[24:25]
	global_load_dwordx4 v[172:175], v200, s[34:35]
	s_nop 0
	global_load_dwordx4 v[168:171], v201, s[42:43]
	s_and_b64 vcc, exec, s[2:3]
	s_cbranch_vccnz .LBB4_946
	s_mov_b64 s[2:3], s[8:9]
	global_store_dwordx2 v193, v[184:185], s[2:3] nt
